# speedup vs baseline: 1.0387x; 1.0114x over previous
.LBB1_12:
	s_or_b64 exec, exec, s[4:5]
	s_lshl_b32 s3, s3, 8
	s_or_b32 s3, s3, s12
	v_or_b32_e32 v2, s3, v220
	v_ashrrev_i32_e32 v3, 31, v2
	v_lshlrev_b64 v[2:3], 8, v[2:3]
	v_lshl_add_u64 v[2:3], s[8:9], 0, v[2:3]
	v_lshlrev_b32_e32 v112, 1, v115
	v_mov_b32_e32 v113, 0
	v_lshl_add_u64 v[2:3], v[2:3], 0, v[112:113]
	s_waitcnt lgkmcnt(0)
	s_barrier
	global_load_dwordx4 v[142:145], v[2:3], off
	global_load_dwordx4 v[146:149], v[2:3], off offset:16
	ds_read_b128 v[150:153], v218
	ds_read_b128 v[154:157], v218 offset:1024
	global_load_dwordx4 v[158:161], v[2:3], off offset:32
	global_load_dwordx4 v[162:165], v[2:3], off offset:48
	global_load_dwordx4 v[166:169], v[2:3], off offset:64
	global_load_dwordx4 v[170:173], v[2:3], off offset:80
	global_load_dwordx4 v[174:177], v[2:3], off offset:96
	global_load_dwordx4 v[178:181], v[2:3], off offset:112
	v_add_u32_e32 v56, v35, v114
	ds_read_b128 v[36:39], v218 offset:8192
	ds_read_b128 v[40:43], v218 offset:9216
	ds_read_b128 v[2:5], v56 offset:54784
	ds_read_b128 v[6:9], v56 offset:54816
	ds_read_b128 v[10:13], v56 offset:54848
	ds_read_b128 v[14:17], v56 offset:54880
	ds_read_b128 v[44:47], v56 offset:54272
	ds_read_b128 v[48:51], v56 offset:54304
	ds_read_b128 v[18:21], v56 offset:54656
	ds_read_b128 v[22:25], v56 offset:54688
	ds_read_b128 v[26:29], v56 offset:54720
	ds_read_b128 v[30:33], v56 offset:54752
	s_movk_i32 s3, 0x3dfd
	v_mov_b32_e32 v221, 0xc807
	s_movk_i32 s20, 0x4480
	s_mov_b32 s21, 0xbc04
	v_add_u32_e32 v35, v35, v115
	s_mov_b32 s4, 0
	s_mov_b32 s18, s4
	s_mov_b32 s19, s4
	s_mov_b32 s5, s4
	s_mov_b32 s6, s4
	s_mov_b32 s7, s4
	s_mov_b32 s8, s4
	s_mov_b32 s9, s4
	s_mov_b32 s10, s4
	s_mov_b32 s11, s4
	s_mov_b32 s12, s4
	s_mov_b32 s13, s4
	s_mov_b32 s14, s4
	s_mov_b32 s15, s4
	s_mov_b32 s16, s4
	s_mov_b32 s17, s4
	s_waitcnt vmcnt(7) lgkmcnt(5)
	v_pk_add_f16 v44, v142, v44
	v_pk_add_f16 v45, v143, v45
	v_pk_add_f16 v46, v144, v46
	v_pk_add_f16 v47, v145, v47
	v_or_b32_e32 v53, 0x80008000, v46
	v_or_b32_e32 v52, 0x80008000, v47
	v_or_b32_e32 v54, 0x80008000, v45
	v_or_b32_e32 v55, 0x80008000, v44
	v_pk_fma_f16 v61, v55, s3, v221 op_sel_hi:[1,0,0]
	v_pk_fma_f16 v62, v54, s3, v221 op_sel_hi:[1,0,0]
	v_pk_fma_f16 v63, v53, s3, v221 op_sel_hi:[1,0,0]
	v_pk_fma_f16 v64, v52, s3, v221 op_sel_hi:[1,0,0]
	v_pk_max_f16 v44, v44, 0
	v_pk_max_f16 v45, v45, 0
	v_pk_max_f16 v46, v46, 0
	v_pk_max_f16 v47, v47, 0
	v_pk_fma_f16 v64, v64, v52, s20 op_sel_hi:[1,1,0]
	v_pk_fma_f16 v63, v63, v53, s20 op_sel_hi:[1,1,0]
	v_pk_fma_f16 v62, v62, v54, s20 op_sel_hi:[1,1,0]
	v_pk_fma_f16 v61, v61, v55, s20 op_sel_hi:[1,1,0]
	v_pk_fma_f16 v62, v62, v54, s21 op_sel_hi:[1,1,0]
	v_pk_fma_f16 v61, v61, v55, s21 op_sel_hi:[1,1,0]
	v_pk_fma_f16 v63, v63, v53, s21 op_sel_hi:[1,1,0]
	v_pk_fma_f16 v64, v64, v52, s21 op_sel_hi:[1,1,0]
	s_waitcnt vmcnt(6) lgkmcnt(4)
	v_pk_add_f16 v48, v146, v48
	v_exp_f16_e32 v68, v61
	v_exp_f16_e32 v69, v62
	v_exp_f16_e32 v70, v63
	v_exp_f16_e32 v71, v64
	v_exp_f16_sdwa v68, v61 dst_sel:WORD_1 dst_unused:UNUSED_PRESERVE src0_sel:WORD_1
	v_exp_f16_sdwa v69, v62 dst_sel:WORD_1 dst_unused:UNUSED_PRESERVE src0_sel:WORD_1
	v_exp_f16_sdwa v70, v63 dst_sel:WORD_1 dst_unused:UNUSED_PRESERVE src0_sel:WORD_1
	v_exp_f16_sdwa v71, v64 dst_sel:WORD_1 dst_unused:UNUSED_PRESERVE src0_sel:WORD_1
	v_pk_add_f16 v49, v147, v49
	v_pk_fma_f16 v47, v52, v71, v47
	v_pk_fma_f16 v46, v53, v70, v46
	v_pk_fma_f16 v45, v54, v69, v45
	v_pk_fma_f16 v44, v55, v68, v44
	v_pk_add_f16 v50, v148, v50
	v_pk_add_f16 v51, v149, v51
	s_waitcnt lgkmcnt(0)
	v_mfma_f32_32x32x16_f16 v[18:33], v[150:153], v[44:47], v[18:33]
	v_or_b32_e32 v57, 0x80008000, v51
	v_or_b32_e32 v58, 0x80008000, v50
	v_or_b32_e32 v59, 0x80008000, v49
	v_or_b32_e32 v60, 0x80008000, v48
	v_pk_fma_f16 v65, v60, s3, v221 op_sel_hi:[1,0,0]
	v_pk_fma_f16 v66, v59, s3, v221 op_sel_hi:[1,0,0]
	v_pk_fma_f16 v67, v58, s3, v221 op_sel_hi:[1,0,0]
	v_mfma_f32_32x32x16_f16 v[2:17], v[36:39], v[44:47], v[2:17]
	v_pk_fma_f16 v52, v57, s3, v221 op_sel_hi:[1,0,0]
	v_pk_fma_f16 v53, v67, v58, s20 op_sel_hi:[1,1,0]
	v_pk_fma_f16 v52, v52, v57, s20 op_sel_hi:[1,1,0]
	v_pk_fma_f16 v54, v66, v59, s20 op_sel_hi:[1,1,0]
	v_pk_fma_f16 v55, v65, v60, s20 op_sel_hi:[1,1,0]
	v_pk_max_f16 v48, v48, 0
	v_pk_max_f16 v49, v49, 0
	v_pk_max_f16 v50, v50, 0
	v_pk_max_f16 v51, v51, 0
	v_pk_fma_f16 v55, v55, v60, s21 op_sel_hi:[1,1,0]
	v_pk_fma_f16 v54, v54, v59, s21 op_sel_hi:[1,1,0]
	v_pk_fma_f16 v36, v53, v58, s21 op_sel_hi:[1,1,0]
	v_pk_fma_f16 v37, v52, v57, s21 op_sel_hi:[1,1,0]
	s_nop 0
	v_exp_f16_e32 v44, v55
	v_exp_f16_e32 v45, v54
	v_exp_f16_e32 v38, v36
	v_exp_f16_e32 v39, v37
	v_exp_f16_sdwa v44, v55 dst_sel:WORD_1 dst_unused:UNUSED_PRESERVE src0_sel:WORD_1
	v_exp_f16_sdwa v45, v54 dst_sel:WORD_1 dst_unused:UNUSED_PRESERVE src0_sel:WORD_1
	v_exp_f16_sdwa v38, v36 dst_sel:WORD_1 dst_unused:UNUSED_PRESERVE src0_sel:WORD_1
	v_exp_f16_sdwa v39, v37 dst_sel:WORD_1 dst_unused:UNUSED_PRESERVE src0_sel:WORD_1
	s_nop 0
	v_pk_fma_f16 v39, v57, v39, v51
	v_pk_fma_f16 v38, v58, v38, v50
	v_pk_fma_f16 v37, v59, v45, v49
	v_pk_fma_f16 v36, v60, v44, v48
	ds_read_b128 v[44:47], v56 offset:54336
	ds_read_b128 v[48:51], v218 offset:2048
	v_mfma_f32_32x32x16_f16 v[18:33], v[154:157], v[36:39], v[18:33]
	v_mfma_f32_32x32x16_f16 v[2:17], v[40:43], v[36:39], v[2:17]
	s_waitcnt vmcnt(5) lgkmcnt(1)
	v_pk_add_f16 v40, v158, v44
	v_pk_add_f16 v41, v159, v45
	v_pk_add_f16 v42, v160, v46
	v_pk_add_f16 v43, v161, v47
	v_or_b32_e32 v45, 0x80008000, v42
	v_or_b32_e32 v44, 0x80008000, v43
	v_or_b32_e32 v46, 0x80008000, v41
	v_or_b32_e32 v47, 0x80008000, v40
	v_pk_fma_f16 v52, v47, s3, v221 op_sel_hi:[1,0,0]
	v_pk_fma_f16 v53, v46, s3, v221 op_sel_hi:[1,0,0]
	v_pk_fma_f16 v54, v45, s3, v221 op_sel_hi:[1,0,0]
	v_pk_fma_f16 v55, v44, s3, v221 op_sel_hi:[1,0,0]
	ds_read_b128 v[36:39], v56 offset:54368
	v_pk_fma_f16 v55, v55, v44, s20 op_sel_hi:[1,1,0]
	v_pk_fma_f16 v54, v54, v45, s20 op_sel_hi:[1,1,0]
	v_pk_fma_f16 v53, v53, v46, s20 op_sel_hi:[1,1,0]
	v_pk_fma_f16 v52, v52, v47, s20 op_sel_hi:[1,1,0]
	v_pk_max_f16 v40, v40, 0
	v_pk_max_f16 v41, v41, 0
	v_pk_max_f16 v42, v42, 0
	v_pk_max_f16 v43, v43, 0
	v_pk_fma_f16 v52, v52, v47, s21 op_sel_hi:[1,1,0]
	v_pk_fma_f16 v53, v53, v46, s21 op_sel_hi:[1,1,0]
	v_pk_fma_f16 v54, v54, v45, s21 op_sel_hi:[1,1,0]
	v_pk_fma_f16 v55, v55, v44, s21 op_sel_hi:[1,1,0]
	s_nop 0
	v_exp_f16_e32 v57, v52
	v_exp_f16_e32 v58, v53
	v_exp_f16_e32 v59, v54
	v_exp_f16_e32 v60, v55
	v_exp_f16_sdwa v57, v52 dst_sel:WORD_1 dst_unused:UNUSED_PRESERVE src0_sel:WORD_1
	v_exp_f16_sdwa v58, v53 dst_sel:WORD_1 dst_unused:UNUSED_PRESERVE src0_sel:WORD_1
	v_exp_f16_sdwa v59, v54 dst_sel:WORD_1 dst_unused:UNUSED_PRESERVE src0_sel:WORD_1
	v_exp_f16_sdwa v60, v55 dst_sel:WORD_1 dst_unused:UNUSED_PRESERVE src0_sel:WORD_1
	s_nop 0
	v_pk_fma_f16 v43, v44, v60, v43
	v_pk_fma_f16 v42, v45, v59, v42
	v_pk_fma_f16 v41, v46, v58, v41
	v_pk_fma_f16 v40, v47, v57, v40
	ds_read_b128 v[44:47], v218 offset:3072
	s_waitcnt vmcnt(4) lgkmcnt(1)
	v_pk_add_f16 v36, v162, v36
	v_mfma_f32_32x32x16_f16 v[18:33], v[48:51], v[40:43], v[18:33]
	ds_read_b128 v[48:51], v218 offset:10240
	ds_read_b128 v[52:55], v218 offset:11264
	v_pk_add_f16 v37, v163, v37
	v_pk_add_f16 v38, v164, v38
	v_pk_add_f16 v39, v165, v39
	s_waitcnt lgkmcnt(1)
	v_mfma_f32_32x32x16_f16 v[2:17], v[48:51], v[40:43], v[2:17]
	v_or_b32_e32 v40, 0x80008000, v39
	v_or_b32_e32 v41, 0x80008000, v38
	v_or_b32_e32 v42, 0x80008000, v37
	v_or_b32_e32 v43, 0x80008000, v36
	v_pk_fma_f16 v48, v43, s3, v221 op_sel_hi:[1,0,0]
	v_pk_fma_f16 v49, v42, s3, v221 op_sel_hi:[1,0,0]
	v_pk_fma_f16 v50, v41, s3, v221 op_sel_hi:[1,0,0]
	v_pk_fma_f16 v51, v40, s3, v221 op_sel_hi:[1,0,0]
	v_pk_fma_f16 v50, v50, v41, s20 op_sel_hi:[1,1,0]
	v_pk_fma_f16 v51, v51, v40, s20 op_sel_hi:[1,1,0]
	v_pk_fma_f16 v49, v49, v42, s20 op_sel_hi:[1,1,0]
	v_pk_fma_f16 v48, v48, v43, s20 op_sel_hi:[1,1,0]
	v_pk_max_f16 v36, v36, 0
	v_pk_max_f16 v37, v37, 0
	v_pk_max_f16 v38, v38, 0
	v_pk_max_f16 v39, v39, 0
	v_pk_fma_f16 v48, v48, v43, s21 op_sel_hi:[1,1,0]
	v_pk_fma_f16 v49, v49, v42, s21 op_sel_hi:[1,1,0]
	v_pk_fma_f16 v50, v50, v41, s21 op_sel_hi:[1,1,0]
	v_pk_fma_f16 v51, v51, v40, s21 op_sel_hi:[1,1,0]
	s_nop 0
	v_exp_f16_e32 v57, v48
	v_exp_f16_e32 v58, v49
	v_exp_f16_e32 v59, v50
	v_exp_f16_e32 v60, v51
	v_exp_f16_sdwa v57, v48 dst_sel:WORD_1 dst_unused:UNUSED_PRESERVE src0_sel:WORD_1
	v_exp_f16_sdwa v58, v49 dst_sel:WORD_1 dst_unused:UNUSED_PRESERVE src0_sel:WORD_1
	v_exp_f16_sdwa v59, v50 dst_sel:WORD_1 dst_unused:UNUSED_PRESERVE src0_sel:WORD_1
	v_exp_f16_sdwa v60, v51 dst_sel:WORD_1 dst_unused:UNUSED_PRESERVE src0_sel:WORD_1
	s_nop 0
	v_pk_fma_f16 v39, v40, v60, v39
	v_pk_fma_f16 v38, v41, v59, v38
	v_pk_fma_f16 v37, v42, v58, v37
	v_pk_fma_f16 v36, v43, v57, v36
	s_nop 1
	v_mfma_f32_32x32x16_f16 v[18:33], v[44:47], v[36:39], v[18:33]
	ds_read_b128 v[40:43], v56 offset:54400
	ds_read_b128 v[44:47], v218 offset:4096
	s_waitcnt vmcnt(3) lgkmcnt(1)
	v_pk_add_f16 v40, v166, v40
	v_pk_add_f16 v41, v167, v41
	v_pk_add_f16 v42, v168, v42
	v_pk_add_f16 v43, v169, v43
	v_mfma_f32_32x32x16_f16 v[2:17], v[52:55], v[36:39], v[2:17]
	v_or_b32_e32 v48, 0x80008000, v43
	v_or_b32_e32 v49, 0x80008000, v42
	v_or_b32_e32 v50, 0x80008000, v41
	v_or_b32_e32 v51, 0x80008000, v40
	v_pk_fma_f16 v52, v51, s3, v221 op_sel_hi:[1,0,0]
	v_pk_fma_f16 v53, v50, s3, v221 op_sel_hi:[1,0,0]
	v_pk_fma_f16 v54, v49, s3, v221 op_sel_hi:[1,0,0]
	v_pk_fma_f16 v55, v48, s3, v221 op_sel_hi:[1,0,0]
	ds_read_b128 v[36:39], v56 offset:54432
	v_pk_fma_f16 v55, v55, v48, s20 op_sel_hi:[1,1,0]
	v_pk_fma_f16 v54, v54, v49, s20 op_sel_hi:[1,1,0]
	v_pk_fma_f16 v53, v53, v50, s20 op_sel_hi:[1,1,0]
	v_pk_fma_f16 v52, v52, v51, s20 op_sel_hi:[1,1,0]
	v_pk_max_f16 v40, v40, 0
	v_pk_max_f16 v41, v41, 0
	v_pk_max_f16 v42, v42, 0
	v_pk_max_f16 v43, v43, 0
	v_pk_fma_f16 v52, v52, v51, s21 op_sel_hi:[1,1,0]
	v_pk_fma_f16 v53, v53, v50, s21 op_sel_hi:[1,1,0]
	v_pk_fma_f16 v54, v54, v49, s21 op_sel_hi:[1,1,0]
	v_pk_fma_f16 v55, v55, v48, s21 op_sel_hi:[1,1,0]
	s_nop 0
	v_exp_f16_e32 v57, v52
	v_exp_f16_e32 v58, v53
	v_exp_f16_e32 v59, v54
	v_exp_f16_e32 v60, v55
	v_exp_f16_sdwa v57, v52 dst_sel:WORD_1 dst_unused:UNUSED_PRESERVE src0_sel:WORD_1
	v_exp_f16_sdwa v58, v53 dst_sel:WORD_1 dst_unused:UNUSED_PRESERVE src0_sel:WORD_1
	v_exp_f16_sdwa v59, v54 dst_sel:WORD_1 dst_unused:UNUSED_PRESERVE src0_sel:WORD_1
	v_exp_f16_sdwa v60, v55 dst_sel:WORD_1 dst_unused:UNUSED_PRESERVE src0_sel:WORD_1
	s_nop 0
	v_pk_fma_f16 v43, v48, v60, v43
	v_pk_fma_f16 v42, v49, v59, v42
	v_pk_fma_f16 v41, v50, v58, v41
	v_pk_fma_f16 v40, v51, v57, v40
	ds_read_b128 v[48:51], v218 offset:5120
	s_waitcnt vmcnt(2) lgkmcnt(1)
	v_pk_add_f16 v36, v170, v36
	v_mfma_f32_32x32x16_f16 v[18:33], v[44:47], v[40:43], v[18:33]
	ds_read_b128 v[44:47], v218 offset:12288
	ds_read_b128 v[52:55], v218 offset:13312
	v_pk_add_f16 v37, v171, v37
	v_pk_add_f16 v38, v172, v38
	v_pk_add_f16 v39, v173, v39
	s_waitcnt lgkmcnt(1)
	v_mfma_f32_32x32x16_f16 v[2:17], v[44:47], v[40:43], v[2:17]
	v_or_b32_e32 v40, 0x80008000, v39
	v_or_b32_e32 v41, 0x80008000, v38
	v_or_b32_e32 v42, 0x80008000, v37
	v_or_b32_e32 v43, 0x80008000, v36
	v_pk_fma_f16 v44, v43, s3, v221 op_sel_hi:[1,0,0]
	v_pk_fma_f16 v45, v42, s3, v221 op_sel_hi:[1,0,0]
	v_pk_fma_f16 v46, v41, s3, v221 op_sel_hi:[1,0,0]
	v_pk_fma_f16 v47, v40, s3, v221 op_sel_hi:[1,0,0]
	v_pk_fma_f16 v46, v46, v41, s20 op_sel_hi:[1,1,0]
	v_pk_fma_f16 v47, v47, v40, s20 op_sel_hi:[1,1,0]
	v_pk_fma_f16 v45, v45, v42, s20 op_sel_hi:[1,1,0]
	v_pk_fma_f16 v44, v44, v43, s20 op_sel_hi:[1,1,0]
	v_pk_fma_f16 v45, v45, v42, s21 op_sel_hi:[1,1,0]
	v_pk_fma_f16 v44, v44, v43, s21 op_sel_hi:[1,1,0]
	v_pk_fma_f16 v46, v46, v41, s21 op_sel_hi:[1,1,0]
	v_pk_fma_f16 v47, v47, v40, s21 op_sel_hi:[1,1,0]
	v_pk_max_f16 v36, v36, 0
	v_pk_max_f16 v37, v37, 0
	v_pk_max_f16 v38, v38, 0
	v_pk_max_f16 v39, v39, 0
	v_exp_f16_e32 v57, v44
	v_exp_f16_e32 v58, v45
	v_exp_f16_e32 v59, v46
	v_exp_f16_e32 v60, v47
	v_exp_f16_sdwa v57, v44 dst_sel:WORD_1 dst_unused:UNUSED_PRESERVE src0_sel:WORD_1
	v_exp_f16_sdwa v58, v45 dst_sel:WORD_1 dst_unused:UNUSED_PRESERVE src0_sel:WORD_1
	v_exp_f16_sdwa v59, v46 dst_sel:WORD_1 dst_unused:UNUSED_PRESERVE src0_sel:WORD_1
	v_exp_f16_sdwa v60, v47 dst_sel:WORD_1 dst_unused:UNUSED_PRESERVE src0_sel:WORD_1
	s_nop 0
	v_pk_fma_f16 v39, v40, v60, v39
	v_pk_fma_f16 v38, v41, v59, v38
	v_pk_fma_f16 v37, v42, v58, v37
	v_pk_fma_f16 v36, v43, v57, v36
	ds_read_b128 v[40:43], v56 offset:54464
	ds_read_b128 v[44:47], v218 offset:6144
	v_mfma_f32_32x32x16_f16 v[18:33], v[48:51], v[36:39], v[18:33]
	s_waitcnt vmcnt(1) lgkmcnt(1)
	v_pk_add_f16 v40, v174, v40
	v_pk_add_f16 v41, v175, v41
	v_pk_add_f16 v42, v176, v42
	v_pk_add_f16 v43, v177, v43
	v_or_b32_e32 v49, 0x80008000, v42
	v_mfma_f32_32x32x16_f16 v[2:17], v[52:55], v[36:39], v[2:17]
	v_or_b32_e32 v48, 0x80008000, v43
	v_or_b32_e32 v50, 0x80008000, v41
	v_or_b32_e32 v51, 0x80008000, v40
	v_pk_fma_f16 v52, v51, s3, v221 op_sel_hi:[1,0,0]
	v_pk_fma_f16 v53, v50, s3, v221 op_sel_hi:[1,0,0]
	v_pk_fma_f16 v54, v49, s3, v221 op_sel_hi:[1,0,0]
	v_pk_fma_f16 v55, v48, s3, v221 op_sel_hi:[1,0,0]
	ds_read_b128 v[36:39], v56 offset:54496
	v_pk_fma_f16 v55, v55, v48, s20 op_sel_hi:[1,1,0]
	v_pk_fma_f16 v54, v54, v49, s20 op_sel_hi:[1,1,0]
	v_pk_fma_f16 v53, v53, v50, s20 op_sel_hi:[1,1,0]
	v_pk_fma_f16 v52, v52, v51, s20 op_sel_hi:[1,1,0]
	v_pk_max_f16 v40, v40, 0
	v_pk_max_f16 v41, v41, 0
	v_pk_max_f16 v42, v42, 0
	v_pk_max_f16 v43, v43, 0
	v_pk_fma_f16 v52, v52, v51, s21 op_sel_hi:[1,1,0]
	v_pk_fma_f16 v53, v53, v50, s21 op_sel_hi:[1,1,0]
	v_pk_fma_f16 v54, v54, v49, s21 op_sel_hi:[1,1,0]
	v_pk_fma_f16 v55, v55, v48, s21 op_sel_hi:[1,1,0]
	s_waitcnt vmcnt(0) lgkmcnt(0)
	v_pk_add_f16 v36, v178, v36
	v_exp_f16_e32 v56, v52
	v_exp_f16_e32 v57, v53
	v_exp_f16_e32 v58, v54
	v_exp_f16_e32 v59, v55
	v_exp_f16_sdwa v56, v52 dst_sel:WORD_1 dst_unused:UNUSED_PRESERVE src0_sel:WORD_1
	v_exp_f16_sdwa v57, v53 dst_sel:WORD_1 dst_unused:UNUSED_PRESERVE src0_sel:WORD_1
	v_exp_f16_sdwa v58, v54 dst_sel:WORD_1 dst_unused:UNUSED_PRESERVE src0_sel:WORD_1
	v_exp_f16_sdwa v59, v55 dst_sel:WORD_1 dst_unused:UNUSED_PRESERVE src0_sel:WORD_1
	v_pk_add_f16 v37, v179, v37
	v_pk_fma_f16 v43, v48, v59, v43
	v_pk_fma_f16 v42, v49, v58, v42
	v_pk_fma_f16 v41, v50, v57, v41
	v_pk_fma_f16 v40, v51, v56, v40
	ds_read_b128 v[48:51], v218 offset:7168
	v_pk_add_f16 v38, v180, v38
	v_mfma_f32_32x32x16_f16 v[18:33], v[44:47], v[40:43], v[18:33]
	ds_read_b128 v[44:47], v218 offset:14336
	ds_read_b128 v[52:55], v218 offset:15360
	v_pk_add_f16 v39, v181, v39
	s_waitcnt lgkmcnt(1)
	v_mfma_f32_32x32x16_f16 v[2:17], v[44:47], v[40:43], v[2:17]
	v_or_b32_e32 v40, 0x80008000, v39
	v_or_b32_e32 v41, 0x80008000, v38
	v_or_b32_e32 v42, 0x80008000, v37
	v_or_b32_e32 v43, 0x80008000, v36
	v_pk_fma_f16 v44, v43, s3, v221 op_sel_hi:[1,0,0]
	v_pk_fma_f16 v45, v42, s3, v221 op_sel_hi:[1,0,0]
	v_pk_fma_f16 v46, v41, s3, v221 op_sel_hi:[1,0,0]
	v_pk_fma_f16 v47, v40, s3, v221 op_sel_hi:[1,0,0]
	v_pk_fma_f16 v46, v46, v41, s20 op_sel_hi:[1,1,0]
	v_pk_fma_f16 v47, v47, v40, s20 op_sel_hi:[1,1,0]
	v_pk_fma_f16 v45, v45, v42, s20 op_sel_hi:[1,1,0]
	v_pk_fma_f16 v44, v44, v43, s20 op_sel_hi:[1,1,0]
	v_pk_max_f16 v36, v36, 0
	v_pk_max_f16 v37, v37, 0
	v_pk_max_f16 v38, v38, 0
	v_pk_max_f16 v39, v39, 0
	v_pk_fma_f16 v44, v44, v43, s21 op_sel_hi:[1,1,0]
	v_pk_fma_f16 v45, v45, v42, s21 op_sel_hi:[1,1,0]
	v_pk_fma_f16 v46, v46, v41, s21 op_sel_hi:[1,1,0]
	v_pk_fma_f16 v47, v47, v40, s21 op_sel_hi:[1,1,0]
	s_nop 0
	v_exp_f16_e32 v56, v44
	v_exp_f16_e32 v57, v45
	v_exp_f16_e32 v58, v46
	v_exp_f16_e32 v59, v47
	v_exp_f16_sdwa v56, v44 dst_sel:WORD_1 dst_unused:UNUSED_PRESERVE src0_sel:WORD_1
	v_exp_f16_sdwa v57, v45 dst_sel:WORD_1 dst_unused:UNUSED_PRESERVE src0_sel:WORD_1
	v_exp_f16_sdwa v58, v46 dst_sel:WORD_1 dst_unused:UNUSED_PRESERVE src0_sel:WORD_1
	v_exp_f16_sdwa v59, v47 dst_sel:WORD_1 dst_unused:UNUSED_PRESERVE src0_sel:WORD_1
	s_nop 0
	v_pk_fma_f16 v39, v40, v59, v39
	v_pk_fma_f16 v38, v41, v58, v38
	v_pk_fma_f16 v37, v42, v57, v37
	v_pk_fma_f16 v36, v43, v56, v36
	s_nop 1
	v_mfma_f32_32x32x16_f16 v[18:33], v[48:51], v[36:39], v[18:33]
	s_waitcnt lgkmcnt(0)
	v_mfma_f32_32x32x16_f16 v[2:17], v[52:55], v[36:39], v[2:17]
	s_setprio 2
	ds_read_b128 v[48:51], v218 offset:16384
	ds_read_b128 v[52:55], v218 offset:17408
	ds_read_b128 v[36:39], v35 offset:54528
	s_nop 6
	v_cvt_pk_f16_f32 v122, v18, v19
	v_mov_b32_e32 v18, 0x1ec00
	v_cvt_pk_f16_f32 v116, v24, v25
	v_cvt_pk_f16_f32 v117, v22, v23
	v_cvt_pk_f16_f32 v120, v20, v21
	v_lshl_add_u32 v222, v34, 2, v18
	ds_read_b128 v[56:59], v35 offset:54544
	ds_read_b128 v[60:63], v35 offset:54560
	ds_read_b128 v[64:67], v35 offset:54576
	s_waitcnt lgkmcnt(3)
	v_pk_add_f16 v25, v39, v116
	v_pk_add_f16 v24, v38, v117
	v_pk_add_f16 v23, v37, v120
	v_pk_add_f16 v22, v36, v122
	v_cvt_pk_f16_f32 v112, v32, v33
	ds_read_b128 v[32:35], v222
	ds_read_b128 v[36:39], v222 offset:1024
	ds_read_b128 v[40:43], v222 offset:2048
	ds_read_b128 v[44:47], v222 offset:3072
	s_waitcnt lgkmcnt(0)
	v_mfma_f32_32x32x16_f16 v[32:47], v[48:51], v[22:25], v[32:47]
	v_cvt_pk_f16_f32 v128, v30, v31
	v_cvt_pk_f16_f32 v129, v28, v29
	v_cvt_pk_f16_f32 v130, v26, v27
	v_pk_add_f16 v21, v59, v112
	v_pk_add_f16 v20, v58, v128
	v_pk_add_f16 v19, v57, v129
	v_pk_add_f16 v18, v56, v130
	v_cvt_pk_f16_f32 v118, v8, v9
	v_cvt_pk_f16_f32 v121, v6, v7
	ds_read_b128 v[6:9], v218 offset:18432
	v_mfma_f32_32x32x16_f16 v[32:47], v[52:55], v[18:21], v[32:47]
	v_cvt_pk_f16_f32 v124, v4, v5
	v_cvt_pk_f16_f32 v126, v2, v3
	v_pk_add_f16 v29, v63, v118
	v_pk_add_f16 v28, v62, v121
	v_pk_add_f16 v27, v61, v124
	v_pk_add_f16 v26, v60, v126
	ds_read_b128 v[2:5], v218 offset:19456
	ds_read_b128 v[48:51], v218 offset:20480
	s_waitcnt lgkmcnt(2)
	v_mfma_f32_32x32x16_f16 v[32:47], v[6:9], v[26:29], v[32:47]
	v_cvt_pk_f16_f32 v119, v16, v17
	v_cvt_pk_f16_f32 v123, v14, v15
	v_cvt_pk_f16_f32 v125, v12, v13
	v_cvt_pk_f16_f32 v127, v10, v11
	v_pk_add_f16 v67, v67, v119
	v_pk_add_f16 v66, v66, v123
	v_pk_add_f16 v65, v65, v125
	v_pk_add_f16 v64, v64, v127
	s_waitcnt lgkmcnt(1)
	s_nop 0
	v_mfma_f32_32x32x16_f16 v[32:47], v[2:5], v[64:67], v[32:47]
	ds_read_b128 v[2:5], v222 offset:4096
	ds_read_b128 v[6:9], v222 offset:5120
	ds_read_b128 v[10:13], v222 offset:6144
	ds_read_b128 v[14:17], v222 offset:7168
	ds_read_b128 v[52:55], v218 offset:21504
	s_nop 6
	v_cvt_pk_f16_f32 v30, v38, v39
	s_waitcnt lgkmcnt(1)
	v_mfma_f32_32x32x16_f16 v[2:17], v[48:51], v[22:25], v[2:17]
	v_pk_max_f16 v99, v30, 0
	v_cvt_pk_f16_f32 v30, v36, v37
	v_pk_max_f16 v98, v30, 0
	v_cvt_pk_f16_f32 v30, v34, v35
	v_pk_max_f16 v97, v30, 0
	v_cvt_pk_f16_f32 v30, v32, v33
	v_pk_max_f16 v96, v30, 0
	s_waitcnt lgkmcnt(0)
	v_mfma_f32_32x32x16_f16 v[2:17], v[52:55], v[18:21], v[2:17]
	ds_read_b128 v[48:51], v218 offset:22528
	ds_read_b128 v[52:55], v218 offset:23552
	ds_read_b128 v[68:71], v218 offset:24576
	v_cvt_pk_f16_f32 v38, v46, v47
	v_pk_max_f16 v103, v38, 0
	s_waitcnt lgkmcnt(2)
	v_mfma_f32_32x32x16_f16 v[2:17], v[48:51], v[26:29], v[2:17]
	s_waitcnt lgkmcnt(1)
	v_mfma_f32_32x32x16_f16 v[2:17], v[52:55], v[64:67], v[2:17]
	ds_read_b128 v[48:51], v222 offset:8192
	ds_read_b128 v[52:55], v222 offset:9216
	ds_read_b128 v[56:59], v222 offset:10240
	ds_read_b128 v[60:63], v222 offset:11264
	ds_read_b128 v[72:75], v218 offset:25600
	ds_read_b128 v[34:37], v218 offset:28672
	s_nop 5
	v_cvt_pk_f16_f32 v8, v8, v9
	s_waitcnt lgkmcnt(2)
	v_mfma_f32_32x32x16_f16 v[48:63], v[68:71], v[22:25], v[48:63]
	ds_read_b128 v[68:71], v218 offset:26624
	v_cvt_pk_f16_f32 v6, v6, v7
	v_pk_max_f16 v107, v8, 0
	v_pk_max_f16 v106, v6, 0
	v_cvt_pk_f16_f32 v8, v4, v5
	v_cvt_pk_f16_f32 v2, v2, v3
	v_pk_max_f16 v104, v2, 0
	s_waitcnt lgkmcnt(2)
	v_mfma_f32_32x32x16_f16 v[48:63], v[72:75], v[18:21], v[48:63]
	ds_read_b128 v[72:75], v218 offset:27648
	ds_read_b128 v[80:83], v222 offset:12288
	ds_read_b128 v[84:87], v222 offset:13312
	ds_read_b128 v[88:91], v222 offset:14336
	ds_read_b128 v[92:95], v222 offset:15360
	ds_read_b128 v[30:33], v218 offset:29696
	ds_read_b128 v[4:7], v218 offset:31744
	v_cvt_pk_f16_f32 v2, v16, v17
	v_pk_max_f16 v111, v2, 0
	v_cvt_pk_f16_f32 v2, v14, v15
	s_waitcnt lgkmcnt(2)
	v_mfma_f32_32x32x16_f16 v[80:95], v[34:37], v[22:25], v[80:95]
	v_cvt_pk_f16_f32 v22, v44, v45
	v_pk_max_f16 v102, v22, 0
	v_cvt_pk_f16_f32 v22, v42, v43
	v_pk_max_f16 v101, v22, 0
	ds_read_b128 v[22:25], v218 offset:30720
	v_pk_max_f16 v105, v8, 0
	v_pk_max_f16 v110, v2, 0
	s_waitcnt lgkmcnt(2)
	v_mfma_f32_32x32x16_f16 v[80:95], v[30:33], v[18:21], v[80:95]
	v_cvt_pk_f16_f32 v34, v40, v41
	v_pk_max_f16 v100, v34, 0
	s_waitcnt lgkmcnt(0)
	v_mfma_f32_32x32x16_f16 v[80:95], v[22:25], v[26:29], v[80:95]
	v_mfma_f32_32x32x16_f16 v[48:63], v[68:71], v[26:29], v[48:63]
	v_mfma_f32_32x32x16_f16 v[80:95], v[4:7], v[64:67], v[80:95]
	ds_read_b128 v[2:5], v218 offset:33792
	ds_read_b128 v[6:9], v218 offset:34816
	ds_read_b128 v[14:17], v218 offset:32768
	v_mfma_f32_32x32x16_f16 v[48:63], v[72:75], v[64:67], v[48:63]
	v_mov_b64_e32 v[78:79], s[18:19]
	v_mov_b64_e32 v[76:77], s[16:17]
	v_mov_b64_e32 v[74:75], s[14:15]
	v_mov_b64_e32 v[72:73], s[12:13]
	v_mov_b64_e32 v[70:71], s[10:11]
	v_mov_b64_e32 v[68:69], s[8:9]
	v_mov_b64_e32 v[66:67], s[6:7]
	v_mov_b64_e32 v[64:65], s[4:5]
	s_waitcnt lgkmcnt(0)
	s_nop 1
	v_mfma_f32_32x32x16_f16 v[18:33], v[14:17], v[96:99], v[64:79]
	s_nop 1
	s_mov_b32 s5, 0xd680
	v_mfma_f32_32x32x16_f16 v[18:33], v[2:5], v[100:103], v[18:33]
	v_cvt_pk_f16_f32 v2, v12, v13
	v_pk_max_f16 v109, v2, 0
	v_cvt_pk_f16_f32 v2, v10, v11
	v_pk_max_f16 v108, v2, 0
	v_cvt_pk_f16_f32 v2, v54, v55
	v_pk_max_f16 v55, v2, 0
	ds_read_b128 v[2:5], v218 offset:35840
	v_mfma_f32_32x32x16_f16 v[18:33], v[6:9], v[104:107], v[18:33]
	v_cvt_pk_f16_f32 v6, v52, v53
	v_pk_max_f16 v54, v6, 0
	v_cvt_pk_f16_f32 v6, v50, v51
	v_pk_max_f16 v53, v6, 0
	v_cvt_pk_f16_f32 v6, v48, v49
	v_pk_max_f16 v52, v6, 0
	ds_read_b128 v[6:9], v218 offset:36864
	s_waitcnt lgkmcnt(1)
	v_mfma_f32_32x32x16_f16 v[18:33], v[2:5], v[108:111], v[18:33]
	v_cvt_pk_f16_f32 v2, v62, v63
	v_pk_max_f16 v63, v2, 0
	v_cvt_pk_f16_f32 v2, v60, v61
	v_pk_max_f16 v62, v2, 0
	v_cvt_pk_f16_f32 v2, v58, v59
	v_pk_max_f16 v61, v2, 0
	ds_read_b128 v[2:5], v218 offset:37888
	s_waitcnt lgkmcnt(1)
	v_mfma_f32_32x32x16_f16 v[18:33], v[6:9], v[52:55], v[18:33]
	v_cvt_pk_f16_f32 v6, v56, v57
	v_pk_max_f16 v60, v6, 0
	v_cvt_pk_f16_f32 v6, v86, v87
	v_pk_max_f16 v59, v6, 0
	v_cvt_pk_f16_f32 v6, v84, v85
	v_pk_max_f16 v58, v6, 0
	ds_read_b128 v[6:9], v218 offset:38912
	s_waitcnt lgkmcnt(1)
	v_mfma_f32_32x32x16_f16 v[18:33], v[2:5], v[60:63], v[18:33]
	v_cvt_pk_f16_f32 v2, v82, v83
	v_pk_max_f16 v57, v2, 0
	v_cvt_pk_f16_f32 v2, v80, v81
	v_pk_max_f16 v56, v2, 0
	v_cvt_pk_f16_f32 v2, v94, v95
	v_pk_max_f16 v83, v2, 0
	ds_read_b128 v[2:5], v218 offset:39936
	s_waitcnt lgkmcnt(1)
	v_mfma_f32_32x32x16_f16 v[18:33], v[6:9], v[56:59], v[18:33]
	v_cvt_pk_f16_f32 v6, v92, v93
	v_pk_max_f16 v82, v6, 0
	v_cvt_pk_f16_f32 v6, v90, v91
	v_pk_max_f16 v81, v6, 0
	v_cvt_pk_f16_f32 v6, v88, v89
	v_pk_max_f16 v80, v6, 0
	ds_read_b128 v[6:9], v218 offset:41984
	s_waitcnt lgkmcnt(1)
	v_mfma_f32_32x32x16_f16 v[18:33], v[2:5], v[80:83], v[18:33]
	ds_read_b128 v[2:5], v218 offset:40960
	s_nop 10
	v_xor_b32_e32 v17, 0x80000000, v33
	v_xor_b32_e32 v16, 0x80000000, v32
	v_xor_b32_e32 v15, 0x80000000, v31
	v_xor_b32_e32 v14, 0x80000000, v30
	ds_read_b128 v[30:33], v218 offset:43008
	s_waitcnt lgkmcnt(1)
	s_nop 1
	v_mfma_f32_32x32x16_f16 v[34:49], v[2:5], v[96:99], v[64:79]
	s_nop 1
	v_xor_b32_e32 v11, 0x80000000, v27
	v_mfma_f32_32x32x16_f16 v[34:49], v[6:9], v[100:103], v[34:49]
	v_xor_b32_e32 v10, 0x80000000, v26
	v_xor_b32_e32 v9, 0x80000000, v25
	v_xor_b32_e32 v8, 0x80000000, v24
	ds_read_b128 v[24:27], v218 offset:44032
	v_xor_b32_e32 v5, 0x80000000, v21
	v_xor_b32_e32 v4, 0x80000000, v20
	v_xor_b32_e32 v3, 0x80000000, v19
	s_waitcnt lgkmcnt(1)
	v_mfma_f32_32x32x16_f16 v[34:49], v[30:33], v[104:107], v[34:49]
	v_xor_b32_e32 v2, 0x80000000, v18
	ds_read_b128 v[18:21], v218 offset:45056
	v_xor_b32_e32 v7, 0x80000000, v23
	v_xor_b32_e32 v6, 0x80000000, v22
	v_exp_f32 v64, v113
	v_exp_f32 v65, v113
	v_exp_f32 v66, v113
	v_exp_f32 v67, v113
	v_exp_f32 v68, v113
	v_exp_f32 v69, v113
	v_exp_f32 v70, v113
	v_exp_f32 v71, v113
	v_exp_f32 v72, v113
	v_exp_f32 v73, v113
	v_exp_f32 v74, v113
	v_exp_f32 v75, v113
	v_exp_f32 v76, v113
	v_exp_f32 v77, v113
	v_exp_f32 v78, v113
	v_exp_f32 v79, v113
	v_xor_b32_e32 v13, 0x80000000, v29
	v_pk_add_f32 v[32:33], v[78:79], 0 op_sel_hi:[1,0]
	s_waitcnt lgkmcnt(1)
	v_mfma_f32_32x32x16_f16 v[34:49], v[24:27], v[108:111], v[34:49]
	ds_read_b128 v[22:25], v218 offset:46080
	v_xor_b32_e32 v12, 0x80000000, v28
	v_fma_mix_f32 v216, v64, v122, v113 op_sel:[0,0,0] op_sel_hi:[0,1,0]
	v_fma_mix_f32 v217, v65, v122, v113 op_sel:[0,1,0] op_sel_hi:[0,1,0]
	v_add_f32_e64 v30, v76, 0
	v_add_f32_e64 v31, v77, 0
	v_add_f32_e64 v28, v74, 0
	v_add_f32_e64 v29, v75, 0
	v_pk_add_f32 v[26:27], v[72:73], 0 op_sel_hi:[1,0]
	s_waitcnt lgkmcnt(1)
	v_mfma_f32_32x32x16_f16 v[34:49], v[18:21], v[52:55], v[34:49]
	ds_read_b128 v[18:21], v218 offset:47104
	ds_read_b128 v[50:53], v218 offset:48128
	v_fma_mix_f32 v206, v64, v126, v113 op_sel:[0,0,0] op_sel_hi:[0,1,0]
	v_fma_mix_f32 v207, v65, v126, v113 op_sel:[0,1,0] op_sel_hi:[0,1,0]
	v_fma_mix_f32 v214, v66, v120, v113 op_sel:[0,0,0] op_sel_hi:[0,1,0]
	v_fma_mix_f32 v215, v67, v120, v113 op_sel:[0,1,0] op_sel_hi:[0,1,0]
	v_fma_mix_f32 v212, v68, v117, v113 op_sel:[0,0,0] op_sel_hi:[0,1,0]
	s_waitcnt lgkmcnt(2)
	v_mfma_f32_32x32x16_f16 v[34:49], v[22:25], v[60:63], v[34:49]
	v_add_f32_e64 v24, v70, 0
	v_add_f32_e64 v25, v71, 0
	v_add_f32_e64 v22, v68, 0
	v_add_f32_e64 v23, v69, 0
	v_fma_mix_f32 v213, v69, v117, v113 op_sel:[0,1,0] op_sel_hi:[0,1,0]
	v_fma_mix_f32 v210, v70, v116, v113 op_sel:[0,0,0] op_sel_hi:[0,1,0]
	v_fma_mix_f32 v211, v71, v116, v113 op_sel:[0,1,0] op_sel_hi:[0,1,0]
	v_fma_mix_f32 v208, v72, v130, v113 op_sel:[0,0,0] op_sel_hi:[0,1,0]
	v_fma_mix_f32 v209, v73, v130, v113 op_sel:[0,1,0] op_sel_hi:[0,1,0]
	s_waitcnt lgkmcnt(1)
	v_mfma_f32_32x32x16_f16 v[34:49], v[18:21], v[56:59], v[34:49]
	v_add_f32_e64 v20, v66, 0
	v_add_f32_e64 v21, v67, 0
	v_add_f32_e64 v18, v64, 0
	v_add_f32_e64 v19, v65, 0
	v_fma_mix_f32 v204, v74, v129, v113 op_sel:[0,0,0] op_sel_hi:[0,1,0]
	v_fma_mix_f32 v205, v75, v129, v113 op_sel:[0,1,0] op_sel_hi:[0,1,0]
	v_fma_mix_f32 v202, v76, v128, v113 op_sel:[0,0,0] op_sel_hi:[0,1,0]
	v_fma_mix_f32 v203, v77, v128, v113 op_sel:[0,1,0] op_sel_hi:[0,1,0]
	v_fma_mix_f32 v196, v78, v112, v113 op_sel:[0,0,0] op_sel_hi:[0,1,0]
	s_waitcnt lgkmcnt(0)
	v_mfma_f32_32x32x16_f16 v[34:49], v[50:53], v[80:83], v[34:49]
	s_setprio 1
	v_mul_u32_u24_e32 v50, 14, v1
	v_mul_u32_u24_e32 v50, 0x280, v50
	v_or_b32_e32 v51, v50, v115
	v_add_u32_e32 v223, 0xd780, v51
	v_add3_u32 v224, v50, v114, s5
	v_mov_b64_e32 v[64:65], v[32:33]
	s_mov_b32 s5, 0x42200000
	s_nop 4
	v_xor_b32_e32 v49, 0x80000000, v49
	v_xor_b32_e32 v48, 0x80000000, v48
	v_xor_b32_e32 v47, 0x80000000, v47
	v_xor_b32_e32 v46, 0x80000000, v46
	v_xor_b32_e32 v45, 0x80000000, v45
	v_xor_b32_e32 v44, 0x80000000, v44
	v_xor_b32_e32 v43, 0x80000000, v43
	v_xor_b32_e32 v42, 0x80000000, v42
	v_xor_b32_e32 v41, 0x80000000, v41
	v_xor_b32_e32 v40, 0x80000000, v40
	v_xor_b32_e32 v39, 0x80000000, v39
	v_xor_b32_e32 v38, 0x80000000, v38
	v_xor_b32_e32 v37, 0x80000000, v37
	v_xor_b32_e32 v36, 0x80000000, v36
	v_xor_b32_e32 v35, 0x80000000, v35
	v_xor_b32_e32 v34, 0x80000000, v34
	v_mov_b64_e32 v[62:63], v[30:31]
	v_mov_b64_e32 v[60:61], v[28:29]
	v_mov_b64_e32 v[58:59], v[26:27]
	v_mov_b64_e32 v[56:57], v[24:25]
	v_mov_b64_e32 v[54:55], v[22:23]
	v_mov_b64_e32 v[52:53], v[20:21]
	v_mov_b64_e32 v[50:51], v[18:19]
	v_fma_mix_f32 v197, v79, v112, v113 op_sel:[0,1,0] op_sel_hi:[0,1,0]
	v_fma_mix_f32 v200, v66, v124, v113 op_sel:[0,0,0] op_sel_hi:[0,1,0]
	v_fma_mix_f32 v201, v67, v124, v113 op_sel:[0,1,0] op_sel_hi:[0,1,0]
	v_fma_mix_f32 v198, v68, v121, v113 op_sel:[0,0,0] op_sel_hi:[0,1,0]
	v_fma_mix_f32 v199, v69, v121, v113 op_sel:[0,1,0] op_sel_hi:[0,1,0]
	v_fma_mix_f32 v194, v70, v118, v113 op_sel:[0,0,0] op_sel_hi:[0,1,0]
	v_fma_mix_f32 v195, v71, v118, v113 op_sel:[0,1,0] op_sel_hi:[0,1,0]
	v_fma_mix_f32 v192, v72, v127, v113 op_sel:[0,0,0] op_sel_hi:[0,1,0]
	v_fma_mix_f32 v193, v73, v127, v113 op_sel:[0,1,0] op_sel_hi:[0,1,0]
	v_fma_mix_f32 v190, v74, v125, v113 op_sel:[0,0,0] op_sel_hi:[0,1,0]
	v_fma_mix_f32 v191, v75, v125, v113 op_sel:[0,1,0] op_sel_hi:[0,1,0]
	v_fma_mix_f32 v188, v76, v123, v113 op_sel:[0,0,0] op_sel_hi:[0,1,0]
	v_fma_mix_f32 v189, v77, v123, v113 op_sel:[0,1,0] op_sel_hi:[0,1,0]
	v_fma_mix_f32 v186, v78, v119, v113 op_sel:[0,0,0] op_sel_hi:[0,1,0]
	v_fma_mix_f32 v187, v79, v119, v113 op_sel:[0,1,0] op_sel_hi:[0,1,0]
	s_branch .LBB1_14
